# v56 + DSA output stores non-temporal (keep K/V resident in L2)
# baseline (speedup 1.0000x reference)
.LBB0_1071:
	s_or_b64 exec, exec, s[38:39]
	s_waitcnt lgkmcnt(0)
	ds_read_b128 v[2:5], v203 offset:49280
	ds_read_b128 v[6:9], v203 offset:49312
	s_lshl_b32 s29, s31, 12
	v_lshl_or_b32 v49, v236, 1, s29
	v_add_u32_e32 v49, v49, v242
	s_waitcnt lgkmcnt(1)
	v_rcp_f32_e32 v0, v2
	v_rcp_f32_e32 v10, v3
	v_rcp_f32_e32 v11, v4
	v_rcp_f32_e32 v12, v5
	v_mul_f32_e32 v32, v32, v0
	v_mul_f32_e32 v0, v16, v0
	v_cvt_pk_bf16_f32 v0, v0, s0
	s_waitcnt lgkmcnt(0)
	v_rcp_f32_e32 v13, v6
	ds_read_b128 v[2:5], v203 offset:49344
	v_rcp_f32_e32 v14, v7
	v_rcp_f32_e32 v15, v8
	v_rcp_f32_e32 v48, v9
	ds_read_b128 v[6:9], v203 offset:49376
	ds_write_b16 v49, v0 offset:51264
	v_mul_f32_e32 v0, v33, v10
	v_cvt_pk_bf16_f32 v0, v0, s0
	ds_write_b16 v49, v0 offset:51328
	v_mul_f32_e32 v0, v17, v10
	v_cvt_pk_bf16_f32 v0, v0, s0
	ds_write_b16 v49, v0 offset:51392
	v_mul_f32_e32 v0, v34, v11
	v_cvt_pk_bf16_f32 v0, v0, s0
	ds_write_b16 v49, v0 offset:51456
	v_mul_f32_e32 v0, v18, v11
	v_cvt_pk_bf16_f32 v0, v0, s0
	ds_write_b16 v49, v0 offset:51520
	v_mul_f32_e32 v0, v35, v12
	v_cvt_pk_bf16_f32 v0, v0, s0
	ds_write_b16 v49, v0 offset:51584
	v_mul_f32_e32 v0, v19, v12
	v_cvt_pk_bf16_f32 v0, v0, s0
	ds_write_b16 v49, v0 offset:51648
	v_mul_f32_e32 v0, v36, v13
	v_cvt_pk_bf16_f32 v0, v0, s0
	ds_write_b16 v49, v0 offset:52224
	v_mul_f32_e32 v0, v20, v13
	v_cvt_pk_bf16_f32 v0, v0, s0
	ds_write_b16 v49, v0 offset:52288
	v_mul_f32_e32 v0, v37, v14
	v_cvt_pk_bf16_f32 v0, v0, s0
	ds_write_b16 v49, v0 offset:52352
	v_mul_f32_e32 v0, v21, v14
	v_cvt_pk_bf16_f32 v0, v0, s0
	ds_write_b16 v49, v0 offset:52416
	v_mul_f32_e32 v0, v38, v15
	v_cvt_pk_bf16_f32 v0, v0, s0
	ds_write_b16 v49, v0 offset:52480
	v_mul_f32_e32 v0, v22, v15
	v_cvt_pk_bf16_f32 v0, v0, s0
	s_waitcnt lgkmcnt(13)
	v_rcp_f32_e32 v2, v2
	ds_write_b16 v49, v0 offset:52544
	v_mul_f32_e32 v0, v39, v48
	v_cvt_pk_bf16_f32 v0, v0, s0
	ds_write_b16 v49, v0 offset:52608
	v_mul_f32_e32 v0, v23, v48
	v_cvt_pk_bf16_f32 v0, v0, s0
	v_rcp_f32_e32 v3, v3
	ds_write_b16 v49, v0 offset:52672
	v_mul_f32_e32 v0, v40, v2
	v_cvt_pk_bf16_f32 v0, v0, s0
	ds_write_b16 v49, v0 offset:53248
	v_mul_f32_e32 v0, v24, v2
	v_cvt_pk_bf16_f32 v0, v0, s0
	v_rcp_f32_e32 v4, v4
	ds_write_b16 v49, v0 offset:53312
	v_mul_f32_e32 v0, v41, v3
	v_cvt_pk_bf16_f32 v0, v0, s0
	ds_write_b16 v49, v0 offset:53376
	v_mul_f32_e32 v0, v25, v3
	v_cvt_pk_bf16_f32 v0, v0, s0
	v_rcp_f32_e32 v5, v5
	ds_write_b16 v49, v0 offset:53440
	v_mul_f32_e32 v0, v42, v4
	v_cvt_pk_bf16_f32 v0, v0, s0
	ds_write_b16 v49, v0 offset:53504
	v_mul_f32_e32 v0, v26, v4
	v_cvt_pk_bf16_f32 v0, v0, s0
	s_waitcnt lgkmcnt(14)
	v_rcp_f32_e32 v6, v6
	ds_write_b16 v49, v0 offset:53568
	v_mul_f32_e32 v0, v43, v5
	v_cvt_pk_bf16_f32 v0, v0, s0
	ds_write_b16 v49, v0 offset:53632
	v_mul_f32_e32 v0, v27, v5
	v_cvt_pk_bf16_f32 v0, v0, s0
	v_rcp_f32_e32 v7, v7
	ds_write_b16 v49, v0 offset:53696
	v_mul_f32_e32 v0, v44, v6
	v_cvt_pk_bf16_f32 v0, v0, s0
	ds_write_b16 v49, v0 offset:54272
	v_mul_f32_e32 v0, v28, v6
	v_cvt_pk_bf16_f32 v0, v0, s0
	v_rcp_f32_e32 v8, v8
	ds_write_b16 v49, v0 offset:54336
	v_mul_f32_e32 v0, v45, v7
	v_cvt_pk_bf16_f32 v0, v0, s0
	ds_write_b16 v49, v0 offset:54400
	v_mul_f32_e32 v0, v29, v7
	v_cvt_pk_bf16_f32 v0, v0, s0
	v_rcp_f32_e32 v9, v9
	ds_write_b16 v49, v0 offset:54464
	v_mul_f32_e32 v0, v46, v8
	v_cvt_pk_bf16_f32 v0, v0, s0
	ds_write_b16 v49, v0 offset:54528
	v_mul_f32_e32 v0, v30, v8
	v_cvt_pk_bf16_f32 v0, v0, s0
	ds_write_b16 v49, v0 offset:54592
	v_mul_f32_e32 v0, v47, v9
	v_cvt_pk_bf16_f32 v0, v0, s0
	ds_write_b16 v49, v0 offset:54656
	v_mul_f32_e32 v0, v31, v9
	v_cvt_pk_bf16_f32 v32, v32, s0
	v_cvt_pk_bf16_f32 v0, v0, s0
	ds_write_b16 v49, v32 offset:51200
	ds_write_b16 v49, v0 offset:54720
	v_or_b32_e32 v0, s29, v204
	s_waitcnt lgkmcnt(0)
	v_add_u32_e32 v2, v0, v243
	ds_read_b128 v[2:5], v2 offset:51200
	v_add_u32_e32 v6, v0, v244
	ds_read_b128 v[6:9], v6 offset:51200
	v_mov_b32_e32 v205, v1
	v_lshl_add_u64 v[10:11], s[50:51], 0, v[204:205]
	v_mov_b32_e32 v207, v1
	v_lshl_add_u64 v[12:13], v[10:11], 0, v[206:207]
	v_mov_b32_e32 v209, v1
	s_waitcnt lgkmcnt(1)
	global_store_dwordx4 v[12:13], v[2:5], off sc1 nt
	v_mov_b32_e32 v211, v1
	v_lshl_add_u64 v[12:13], v[10:11], 0, v[210:211]
	v_lshl_add_u64 v[2:3], v[10:11], 0, v[208:209]
	s_waitcnt lgkmcnt(0)
	global_store_dwordx4 v[2:3], v[6:9], off sc1 nt
	v_add_u32_e32 v2, v0, v245
	ds_read_b128 v[2:5], v2 offset:51200
	v_add_u32_e32 v0, v0, v246
	ds_read_b128 v[6:9], v0 offset:51200
	v_mov_b32_e32 v213, v1
	s_mov_b64 s[52:53], 0
	s_waitcnt lgkmcnt(1)
	global_store_dwordx4 v[12:13], v[2:5], off sc1 nt
	s_and_b64 vcc, exec, s[54:55]
	s_nop 0
	v_lshl_add_u64 v[2:3], v[10:11], 0, v[212:213]
	s_waitcnt lgkmcnt(0)
	global_store_dwordx4 v[2:3], v[6:9], off sc1 nt
	s_waitcnt lgkmcnt(0)
	s_barrier
	s_cbranch_vccnz .LBB0_1069
